# Fourier stage B output: each wave transposes its 32x32 K and V tiles through a private LDS staging area so the global stores are 16 B per lane with 4 adjacent lanes per row (4 stores of 64 B pieces in
# speedup vs baseline: 1.0076x; 1.0058x over previous
; #define LAS __attribute__((address_space(3)))
;     __device__ __forceinline__ bf16_t* dft() const { return (bf16_t*)(ws + WS_DFT); }
;     __device__ __forceinline__ bf16_t* dn() const { return (bf16_t*)(ws + WS_DN); }
; #define FB_LOAD(u) do { const int _b = (u) >> 9, _k1 = ((u) >> 2) & 127, _cb = (u) & 3; \
;         _Pragma("unroll") for (int _q = 0; _q < 4; ++_q) pf[_q] = *(const bf16x8*)(F.zm() + (size_t)((_b * 128 + _k1) * 64 + (_q & 1) * 32 + sr) * DM + (_q >> 1) * 512 + _cb * 128 + sc); } while (0)
; __device__ __forceinline__ void phase_fft_b(const Frame& F) {
;     const int tid = F.tid, wid = F.wid, lane = F.lane, r32 = lane & 31, hi = lane >> 5;
;     LAS char* Vt = (LAS char*)F.lds;
;     const int sr = tid >> 4, sc = (tid & 15) * 8;
;     const int rb = wid & 1, cq = wid >> 1, k2 = 32 * rb + r32;
;     const bf16_t* dc = F.dft() + 32768; const bf16_t* ds = dc + 4096; const bf16_t* dn = dc + 8192;
;     bf16x8 bc[4], bs[4], bn[4];
; #pragma unroll
;     for (int ks = 0; ks < 4; ++ks) { const int o = k2 * 64 + ks * 16 + hi * 8; bc[ks] = *(const bf16x8*)(dc + o); bs[ks] = *(const bf16x8*)(ds + o); bn[ks] = *(const bf16x8*)(dn + o); }
;     const int NU = NB * 128 * 4;
;     bf16x8 pf[4];
;     ...
;     int u = F.wg, par = 0;
;     if (u < NU) FB_LOAD(u);
.LBB0_508:
	s_andn2_b64 vcc, exec, s[8:9]
	s_cbranch_vccnz .LBB0_585
	v_readlane_b32 s8, v252, 42
	s_waitcnt vmcnt(0)
	v_mov_b32_e32 v2, v0
	v_readlane_b32 s9, v252, 43
	s_andn2_b64 vcc, exec, s[8:9]
	v_readfirstlane_b32 s0, v2
	v_mov_b32_e32 v136, 0xffff8000
	v_mov_b32_e32 v137, 0xffffa000
	v_mov_b32_e32 v138, 0xffffc000
	v_mov_b32_e32 v139, 0xa000
	v_mov_b32_e32 v140, 0xc000
	v_mov_b32_e32 v141, 0x10000
	v_mov_b32_e32 v142, 0x12000
	v_mov_b32_e32 v143, 0x14000
	v_mov_b32_e32 v144, 0x16000
	v_mov_b32_e32 v145, 0x18000
	v_mov_b32_e32 v148, 0x1a000
	v_mov_b32_e32 v149, 0x1c000
	s_cbranch_vccnz .LBB0_516
	s_lshr_b32 s1, s0, 1
	s_add_u32 s8, s56, 0xd0000
	v_and_b32_e32 v1, 31, v2
	s_addc_u32 s9, s57, 0
	v_and_or_b32 v1, s1, 32, v1
	s_add_u32 s18, s56, 0xd2000
	v_bfe_u32 v3, v2, 5, 1
	s_addc_u32 s19, s57, 0
	v_lshlrev_b32_e32 v1, 7, v1
	s_add_u32 s22, s56, 0xd4000
	v_lshl_or_b32 v4, v3, 4, v1
	v_ashrrev_i32_e32 v100, 4, v2
	v_readlane_b32 s1, v253, 1
	s_addc_u32 s23, s57, 0
	v_or_b32_e32 v5, 32, v4
	v_add_u32_e32 v6, s1, v100
	global_load_dwordx4 v[34:37], v4, s[8:9]
	global_load_dwordx4 v[38:41], v4, s[18:19]
	global_load_dwordx4 v[42:45], v4, s[22:23]
	global_load_dwordx4 v[46:49], v5, s[8:9]
	global_load_dwordx4 v[50:53], v5, s[18:19]
	global_load_dwordx4 v[54:57], v5, s[22:23]
	v_or_b32_e32 v5, 64, v4
	s_ashr_i32 s0, s0, 7
	v_ashrrev_i32_e32 v7, 31, v6
	global_load_dwordx4 v[58:61], v5, s[8:9]
	global_load_dwordx4 v[62:65], v5, s[18:19]
	v_or_b32_e32 v4, 0x60, v4
	global_load_dwordx4 v[66:69], v5, s[22:23]
	global_load_dwordx4 v[70:73], v4, s[8:9]
	global_load_dwordx4 v[74:77], v4, s[18:19]
	global_load_dwordx4 v[78:81], v4, s[22:23]
	s_add_u32 s8, s56, 0x3d316100
	v_lshlrev_b64 v[8:9], 11, v[6:7]
	v_add_u32_e32 v6, 32, v6
	v_lshlrev_b32_e32 v5, 3, v2
	s_addc_u32 s9, s57, 0
	v_readlane_b32 s1, v252, 57
	v_ashrrev_i32_e32 v7, 31, v6
	v_and_b32_e32 v4, 0x78, v5
	v_lshl_add_u64 v[8:9], s[8:9], 0, v[8:9]
	s_lshl_b32 s76, s1, 1
	v_lshlrev_b64 v[6:7], 11, v[6:7]
	v_lshl_add_u64 v[8:9], v[8:9], 0, s[76:77]
	v_lshlrev_b32_e32 v146, 1, v4
	v_lshl_add_u64 v[6:7], s[8:9], 0, v[6:7]
	v_lshl_add_u64 v[8:9], v[8:9], 0, v[146:147]
	v_lshl_add_u64 v[6:7], v[6:7], 0, s[76:77]
	v_lshl_add_u64 v[6:7], v[6:7], 0, v[146:147]
	global_load_dwordx4 v[82:85], v[8:9], off
	global_load_dwordx4 v[86:89], v[8:9], off offset:1024
	global_load_dwordx4 v[90:93], v[6:7], off
	global_load_dwordx4 v[94:97], v[6:7], off offset:1024
	v_lshrrev_b32_e32 v7, 1, v100
	v_and_b32_e32 v8, 3, v100
	v_and_b32_e32 v6, 63, v2
	v_and_or_b32 v7, v7, 4, v8
	v_lshlrev_b32_e32 v101, 6, v7
	v_lshlrev_b32_e32 v7, 4, v2
	v_lshlrev_b32_e32 v6, 3, v6
	v_and_b32_e32 v102, 48, v7
	v_and_b32_e32 v8, 24, v6
	v_and_b32_e32 v7, 0xc0, v7
	v_lshlrev_b32_e32 v2, 1, v2
	s_lshl_b32 s1, s0, 9
	v_and_b32_e32 v2, 32, v2
	v_and_b32_e32 v6, 0x100, v6
	v_or3_b32 v7, v7, s1, v8
	v_or3_b32 v103, v7, v2, v6
	v_lshlrev_b32_e32 v2, 2, v3
	v_and_b32_e32 v3, 0xfffff0, v100
	v_lshlrev_b32_e32 v6, 1, v100
	v_and_or_b32 v3, v6, 8, v3
	v_bfe_u32 v5, v5, 5, 2
	v_lshrrev_b32_e32 v3, 1, v3
	v_or_b32_e32 v3, v3, v5
	v_lshlrev_b32_e32 v104, 9, v3
	v_add_u32_e32 v3, 32, v100
	v_and_b32_e32 v6, 0xfffff0, v3
	v_lshlrev_b32_e32 v3, 1, v3
	s_lshl_b32 s18, s0, 5
	v_and_or_b32 v3, v3, 8, v6
	s_ashr_i32 s19, s18, 31
	v_lshrrev_b32_e32 v3, 1, v3
	v_or_b32_e32 v3, v3, v5
	s_add_u32 s22, s56, 0x1c316100
	v_readlane_b32 s24, v254, 62
	v_lshlrev_b32_e32 v105, 9, v3
	s_addc_u32 s23, s57, 0
	s_mov_b32 s0, 0
	v_lshlrev_b32_e32 v98, 1, v4
	v_lshlrev_b32_e32 v146, 1, v2
	v_readlane_b32 s1, v254, 6
	v_readlane_b32 s30, v253, 15
	s_mov_b32 s31, s24
	v_readlane_b32 s25, v254, 63
	v_and_b32_e32 v122, 31, v0
	v_mul_u32_u24_e32 v122, 0x90, v122
	v_bfe_u32 v123, v0, 5, 1
	v_lshl_add_u32 v122, v123, 3, v122
	v_lshrrev_b32_e32 v123, 6, v0
	v_mul_u32_u24_e32 v123, 0x1200, v123
	v_add_u32_e32 v123, 0x12800, v123
	v_add_u32_e32 v122, v122, v123
	v_bfe_u32 v124, v0, 2, 4
	v_mul_u32_u24_e32 v124, 0x90, v124
	v_add_u32_e32 v123, v123, v124
	v_and_b32_e32 v124, 3, v0
	v_lshl_add_u32 v123, v124, 4, v123
	v_bfe_u32 v1, v0, 2, 4
	v_bfe_u32 v124, v0, 6, 1
	v_lshl_or_b32 v1, v124, 5, v1
	v_lshlrev_b32_e32 v1, 7, v1
	v_and_b32_e32 v146, 3, v0
	v_lshlrev_b32_e32 v146, 4, v146
	s_waitcnt vmcnt(0)
	s_branch .LBB0_512
; __device__ __forceinline__ unsigned cvt_pk_bf16(float lo, float hi) { unsigned r; asm volatile("v_cvt_pk_bf16_f32 %0, %1, %2" : "=v"(r) : "v"(lo), "v"(hi)); return r; }
;     __device__ __forceinline__ bf16_t* proj() const { return (bf16_t*)(ws + WS_PROJ); }
; __device__ __forceinline__ int v_rd_base(int lane) { return ((lane & 3) << 3) | (((lane >> 2) & 3) << 6) | (((lane >> 4) & 1) << 5) | (((lane >> 5) & 1) << 8); }
; __device__ __forceinline__ void phase_fft_b(const Frame& F) {
;     ...
;         f32x16 ar = f32x16{}, bi = f32x16{};
;         const int vbP = (int)(uintptr_t)img + ff::v_rd_base(lane) + cq * 512;
;         ff::xt_two<0>(ar, bi, vbP, bc, bs);
;         ff::xt_two<0>(ar, bi, vbP + 16384, bn, bc);
;         bf16_t* op = F.proj() + (size_t)(b * SEQ + k1 + 128 * k2) * INW + cb * 128 + 32 * cq + 4 * hi;
; #pragma unroll
;         for (int g = 0; g < 4; ++g) {
;             u32x2 wa, wb;
;             wa.x = cvt_pk_bf16(ar[4 * g] * 0.011048543456039806f, ar[4 * g + 1] * 0.011048543456039806f); wa.y = cvt_pk_bf16(ar[4 * g + 2] * 0.011048543456039806f, ar[4 * g + 3] * 0.011048543456039806f);
;             wb.x = cvt_pk_bf16(bi[4 * g] * 0.011048543456039806f, bi[4 * g + 1] * 0.011048543456039806f); wb.y = cvt_pk_bf16(bi[4 * g + 2] * 0.011048543456039806f, bi[4 * g + 3] * 0.011048543456039806f);
;             *(u32x2*)(op + C_K + 8 * g) = wa; *(u32x2*)(op + C_V + 8 * g) = wb;
;         }
.LBB0_511:
	v_add_u32_e32 v99, s40, v103
	ds_read_b64_tr_b16 v[2:3], v99 offset:0
	ds_read_b64_tr_b16 v[4:5], v99 offset:0x800
	ds_read_b64_tr_b16 v[106:107], v99 offset:0x1000
	ds_read_b64_tr_b16 v[108:109], v99 offset:0x1800
	ds_read_b64_tr_b16 v[110:111], v99 offset:0x2000
	ds_read_b64_tr_b16 v[112:113], v99 offset:0x2800
	ds_read_b64_tr_b16 v[114:115], v99 offset:0x3000
	ds_read_b64_tr_b16 v[116:117], v99 offset:0x3800
	s_waitcnt lgkmcnt(0)
	s_bfe_u32 s28, s31, 0x70002
	v_mfma_f32_32x32x16_bf16 v[18:33], v[2:5], v[34:37], 0
	v_add_u32_e32 v99, 0x4000, v99
	v_mfma_f32_32x32x16_bf16 v[2:17], v[2:5], v[38:41], 0
	v_mfma_f32_32x32x16_bf16 v[18:33], v[106:109], v[46:49], v[18:33]
	v_mfma_f32_32x32x16_bf16 v[2:17], v[106:109], v[50:53], v[2:17]
	ds_read_b64_tr_b16 v[106:107], v99 offset:0
	ds_read_b64_tr_b16 v[108:109], v99 offset:0x800
	v_mfma_f32_32x32x16_bf16 v[18:33], v[110:113], v[58:61], v[18:33]
	v_mfma_f32_32x32x16_bf16 v[2:17], v[110:113], v[62:65], v[2:17]
	ds_read_b64_tr_b16 v[110:111], v99 offset:0x1000
	ds_read_b64_tr_b16 v[112:113], v99 offset:0x1800
	v_mfma_f32_32x32x16_bf16 v[18:33], v[114:117], v[70:73], v[18:33]
	v_mfma_f32_32x32x16_bf16 v[2:17], v[114:117], v[74:77], v[2:17]
	ds_read_b64_tr_b16 v[114:115], v99 offset:0x2000
	ds_read_b64_tr_b16 v[116:117], v99 offset:0x2800
	ds_read_b64_tr_b16 v[118:119], v99 offset:0x3000
	ds_read_b64_tr_b16 v[120:121], v99 offset:0x3800
	s_waitcnt lgkmcnt(0)
	v_mfma_f32_32x32x16_bf16 v[18:33], v[106:109], v[42:45], v[18:33]
	s_and_b32 s29, s1, 0xffffe000
	s_or_b32 s28, s29, s28
	s_xor_b32 s0, s0, 1
	s_andn2_b64 vcc, exec, s[24:25]
	s_mov_b32 s31, s2
	v_mfma_f32_32x32x16_bf16 v[2:17], v[106:109], v[34:37], v[2:17]
	v_or_b32_e32 v106, s28, v1
	v_ashrrev_i32_e32 v107, 31, v106
	v_lshlrev_b64 v[106:107], 13, v[106:107]
	s_and_b32 s28, s30, 0x180
	v_lshl_add_u64 v[106:107], s[22:23], 0, v[106:107]
	s_lshl_b32 s76, s28, 1
	v_lshl_add_u64 v[106:107], v[106:107], 0, s[76:77]
	v_mfma_f32_32x32x16_bf16 v[18:33], v[110:113], v[54:57], v[18:33]
	v_lshl_add_u64 v[106:107], s[18:19], 1, v[106:107]
	v_lshl_add_u64 v[106:107], v[106:107], 0, v[146:147]
	v_readlane_b32 s28, v254, 7
	s_add_i32 s1, s1, s28
	s_mov_b32 s30, s7
	v_mfma_f32_32x32x16_bf16 v[2:17], v[110:113], v[46:49], v[2:17]
	v_mfma_f32_32x32x16_bf16 v[18:33], v[114:117], v[66:69], v[18:33]
	v_mfma_f32_32x32x16_bf16 v[2:17], v[114:117], v[58:61], v[2:17]
	v_mfma_f32_32x32x16_bf16 v[18:33], v[118:121], v[78:81], v[18:33]
	v_mfma_f32_32x32x16_bf16 v[2:17], v[118:121], v[70:73], v[2:17]
	s_nop 10
	v_mul_f32_e32 v18, 0x3c3504f3, v18
	v_mul_f32_e32 v19, 0x3c3504f3, v19
	v_mul_f32_e32 v20, 0x3c3504f3, v20
	v_mul_f32_e32 v21, 0x3c3504f3, v21
	v_cvt_pk_bf16_f32 v166, v18, v19
	v_cvt_pk_bf16_f32 v167, v20, v21
	ds_write_b64 v122, v[166:167]
	v_mul_f32_e32 v2, 0x3c3504f3, v2
	v_mul_f32_e32 v3, 0x3c3504f3, v3
	v_mul_f32_e32 v4, 0x3c3504f3, v4
	v_mul_f32_e32 v5, 0x3c3504f3, v5
	v_cvt_pk_bf16_f32 v168, v2, v3
	v_cvt_pk_bf16_f32 v169, v4, v5
	ds_write_b64 v122, v[168:169] offset:64
	v_mul_f32_e32 v22, 0x3c3504f3, v22
	v_mul_f32_e32 v23, 0x3c3504f3, v23
	v_mul_f32_e32 v24, 0x3c3504f3, v24
	v_mul_f32_e32 v25, 0x3c3504f3, v25
	v_cvt_pk_bf16_f32 v170, v22, v23
	v_cvt_pk_bf16_f32 v171, v24, v25
	ds_write_b64 v122, v[170:171] offset:16
	v_mul_f32_e32 v6, 0x3c3504f3, v6
	v_mul_f32_e32 v7, 0x3c3504f3, v7
	v_mul_f32_e32 v8, 0x3c3504f3, v8
	v_mul_f32_e32 v9, 0x3c3504f3, v9
	v_cvt_pk_bf16_f32 v172, v6, v7
	v_cvt_pk_bf16_f32 v173, v8, v9
	ds_write_b64 v122, v[172:173] offset:80
	v_mul_f32_e32 v26, 0x3c3504f3, v26
	v_mul_f32_e32 v27, 0x3c3504f3, v27
	v_mul_f32_e32 v28, 0x3c3504f3, v28
	v_mul_f32_e32 v29, 0x3c3504f3, v29
	v_cvt_pk_bf16_f32 v174, v26, v27
	v_cvt_pk_bf16_f32 v175, v28, v29
	ds_write_b64 v122, v[174:175] offset:32
	v_mul_f32_e32 v10, 0x3c3504f3, v10
	v_mul_f32_e32 v11, 0x3c3504f3, v11
	v_mul_f32_e32 v12, 0x3c3504f3, v12
	v_mul_f32_e32 v13, 0x3c3504f3, v13
	v_cvt_pk_bf16_f32 v176, v10, v11
	v_cvt_pk_bf16_f32 v177, v12, v13
	ds_write_b64 v122, v[176:177] offset:96
	v_mul_f32_e32 v30, 0x3c3504f3, v30
	v_mul_f32_e32 v31, 0x3c3504f3, v31
	v_mul_f32_e32 v32, 0x3c3504f3, v32
	v_mul_f32_e32 v33, 0x3c3504f3, v33
	v_cvt_pk_bf16_f32 v178, v30, v31
	v_cvt_pk_bf16_f32 v179, v32, v33
	ds_write_b64 v122, v[178:179] offset:48
	v_mul_f32_e32 v14, 0x3c3504f3, v14
	v_mul_f32_e32 v15, 0x3c3504f3, v15
	v_mul_f32_e32 v16, 0x3c3504f3, v16
	v_mul_f32_e32 v17, 0x3c3504f3, v17
	v_cvt_pk_bf16_f32 v180, v14, v15
	v_cvt_pk_bf16_f32 v181, v16, v17
	ds_write_b64 v122, v[180:181] offset:112
	s_waitcnt lgkmcnt(0)
	ds_read_b128 v[150:153], v123
	ds_read_b128 v[154:157], v123 offset:2304
	ds_read_b128 v[158:161], v123 offset:64
	ds_read_b128 v[162:165], v123 offset:2368
	s_mov_b64 s[28:29], 0x1000000
	v_lshl_add_u64 v[124:125], v[106:107], 0, s[28:29]
	s_waitcnt lgkmcnt(2)
	global_store_dwordx4 v[106:107], v[150:153], off offset:1024
	global_store_dwordx4 v[124:125], v[154:157], off offset:1024
	s_waitcnt lgkmcnt(0)
	global_store_dwordx4 v[106:107], v[158:161], off offset:2048
	global_store_dwordx4 v[124:125], v[162:165], off offset:2048
	s_cbranch_vccz .LBB0_516
.LBB0_512:
	s_lshl_b32 s2, s0, 15
	s_add_i32 s40, s2, 0
	s_add_i32 s2, s31, s96
	v_add_u32_e32 v2, s40, v104
	v_add_u32_e32 v3, s40, v105
	s_cmpk_gt_i32 s2, 0xfff
	v_add3_u32 v2, v2, v101, v102
	v_add3_u32 v3, v3, v101, v102
	s_cselect_b64 s[24:25], -1, 0
	s_cmpk_lt_i32 s2, 0x1000
	s_mov_b64 s[28:29], -1
	s_waitcnt vmcnt(4)
	ds_write_b128 v2, v[82:85]
	ds_write_b128 v3, v[90:93]
	ds_write_b128 v2, v[86:89] offset:16384
	ds_write_b128 v3, v[94:97] offset:16384
	s_waitcnt lgkmcnt(0)
	s_barrier
	s_cbranch_scc1 .LBB0_514
	v_readlane_b32 s7, v254, 4
	s_add_i32 s7, s30, s7
	s_mov_b64 s[28:29], 0
